# deferred expert-weight fill in MoE phases: one ticket atomic per workgroup for all its tickets, no per-ticket barriers
# speedup vs baseline: 1.0596x; 1.0017x over previous
.LBB0_971:
	s_xor_b32 s1, s5, s42
	s_mul_i32 s5, s0, s2
	s_sub_i32 s4, s4, s5
	s_add_i32 s5, s0, 1
	s_sub_i32 s6, s4, s2
	s_cmp_ge_u32 s4, s2
	s_cselect_b32 s0, s5, s0
	s_cselect_b32 s4, s6, s4
	s_add_i32 s5, s0, 1
	s_cmp_ge_u32 s4, s2
	s_cselect_b32 s0, s5, s0
	s_xor_b32 s0, s0, s1
	s_sub_i32 s0, s0, s1
	s_cmp_eq_u32 s0, s3
	s_cbranch_scc1 .LBB0_988
	s_sub_i32 s2, s0, s3
	s_add_u32 s0, s94, 0x1000
	v_readlane_b32 s6, v253, 20
	s_addc_u32 s1, s95, 0
	s_lshl_b32 s4, s6, 14
	s_add_i32 s13, s4, 0
	s_cmp_lt_i32 s2, 0
	s_mul_i32 s12, s2, 3
	s_cselect_b64 s[4:5], -1, 0
	s_lshl_b32 s2, s6, 6
	s_sub_i32 s14, 0, s2
	s_add_u32 s15, s94, 0x27600000
	s_addc_u32 s16, s95, 0
	s_add_i32 s17, 0, 0x20180
	s_mov_b32 s3, 0
	v_mov_b32_e32 v5, 0
	v_mov_b32_e32 v10, s17
	s_mov_b32 s18, 0x8000
	s_mov_b32 s19, 0x10000
	s_mov_b32 s20, 0x18000
	s_mov_b32 s22, 0x20000
	s_mov_b32 s23, 0x28000
	s_mov_b32 s24, 0x30000
	s_mov_b32 s25, 0x38000
	s_mov_b32 s26, 0x40000
	s_mov_b32 s27, 0x48000
	s_mov_b32 s28, 0x50000
	s_mov_b32 s29, 0x58000
	s_mov_b32 s30, 0x60000
	s_mov_b32 s31, 0x68000
	s_mov_b32 s33, 0x70000
	s_mov_b32 s34, 0x78000
	s_mov_b32 s35, 0xc3e00000
	s_mov_b32 s36, 0x80000
	s_mov_b32 s37, 0x90000
	s_mov_b32 s38, 0xa0000
	s_mov_b32 s39, 0xb0000
	s_mov_b32 s41, 0xc0000
	s_mov_b32 s42, 0xd0000
	s_mov_b32 s43, 0xe0000
	s_mov_b32 s44, 0xf0000
	s_xor_b64 s[4:5], s[4:5], -1
	v_mov_b32_e32 v11, 0x43e00000
	s_mov_b32 s45, 0
	s_waitcnt vmcnt(0)
	s_barrier
	v_mbcnt_lo_u32_b32 v0, -1, 0
	v_mbcnt_hi_u32_b32 v0, -1, v0
	s_nop 0
	v_cmp_eq_u32_e32 vcc, s14, v0
	s_and_saveexec_b64 s[6:7], vcc
	s_cbranch_execz .LBB0_979
	s_mov_b64 s[10:11], exec
	v_mbcnt_lo_u32_b32 v0, s10, 0
	v_mbcnt_hi_u32_b32 v0, s11, v0
	v_cmp_eq_u32_e32 vcc, 0, v0
	s_and_saveexec_b64 s[8:9], vcc
	s_cbranch_execz .LBB0_978
	s_lshl_b32 s2, s12, 3
	v_mov_b32_e32 v1, s2
	global_atomic_add v1, v5, v1, s[0:1] sc0

.LBB0_979:
	s_or_b64 exec, exec, s[6:7]
	s_waitcnt lgkmcnt(0)
	s_barrier
	ds_read_b32 v0, v10
	s_mov_b64 s[6:7], -1
	s_waitcnt lgkmcnt(0)
	v_readfirstlane_b32 s8, v0
	s_mov_b32 s100, s8
	s_branch .LBB0_975

.LBB0_975:
	s_lshl_b32 s8, s45, 3
	s_add_i32 s8, s8, s100
	s_mov_b64 s[6:7], -1
	s_cmpk_gt_u32 s8, 0x5fff
	s_cbranch_scc1 .LBB0_974
	v_readlane_b32 s2, v253, 20
	v_mbcnt_lo_u32_b32 v0, -1, 0
	v_mbcnt_hi_u32_b32 v0, -1, v0
	s_add_i32 s8, s8, s2
	v_ashrrev_i32_e32 v12, 3, v0
	v_and_b32_e32 v1, 7, v0
	v_lshlrev_b32_e32 v0, 3, v0
	s_cmpk_gt_i32 s8, 0x3fff
	v_lshlrev_b32_e32 v16, 2, v1
	v_lshlrev_b32_e32 v6, 4, v1
	v_and_b32_e32 v15, 7, v12
	v_lshrrev_b32_e32 v31, 1, v12
	v_add_u32_e32 v30, 8, v12
	v_add_u32_e32 v29, 16, v12
	v_add_u32_e32 v28, 24, v12
	v_add_u32_e32 v27, 32, v12
	v_add_u32_e32 v26, 40, v12
	v_add_u32_e32 v25, 48, v12
	v_add_u32_e32 v24, 56, v12
	v_add_u32_e32 v23, 0x48, v12
	v_add_u32_e32 v22, 0x50, v12
	v_add_u32_e32 v21, 0x58, v12
	v_add_u32_e32 v20, 0x60, v12
	v_add_u32_e32 v19, 0x68, v12
	v_add_u32_e32 v18, 0x70, v12
	v_add_u32_e32 v17, 0x78, v12
	v_and_b32_e32 v13, 24, v0
	v_lshl_add_u32 v14, v1, 11, s13
	s_cbranch_scc0 .LBB0_984
	s_add_i32 s2, s8, 0xffffc000
	s_lshr_b32 s2, s2, 8
	s_addk_i32 s2, 0x60
	v_readlane_b32 s48, v253, 4
	s_lshl_b64 s[6:7], s[2:3], 20
	s_lshl_b64 s[10:11], s[2:3], 22
	v_readlane_b32 s60, v253, 16
	v_readlane_b32 s61, v253, 17
	s_add_u32 s2, s60, s10
	s_addc_u32 s11, s61, s11
	s_add_u32 s6, s15, s6
	s_addc_u32 s7, s16, s7
	s_lshl_b32 s9, s8, 5
	s_and_b32 s9, s9, 0x3e0
	s_bfe_u32 s10, s8, 0x30005
	s_lshl_b32 s46, s9, 2
	v_lshl_add_u32 v0, s10, 7, v12
	s_add_u32 s46, s2, s46
	s_addc_u32 s47, s11, 0
	v_mov_b32_e32 v7, v5
	v_ashrrev_i32_e32 v1, 31, v0
	v_lshl_add_u64 v[2:3], s[46:47], 0, v[6:7]
	v_lshlrev_b64 v[0:1], 12, v[0:1]
	v_lshl_add_u64 v[8:9], v[2:3], 0, v[0:1]
	v_add_co_u32_e32 v32, vcc, s18, v8
	global_load_dwordx4 v[0:3], v[8:9], off nt
	s_nop 0
	v_addc_co_u32_e32 v33, vcc, 0, v9, vcc
	v_add_co_u32_e32 v36, vcc, s19, v8
	global_load_dwordx4 v[32:35], v[32:33], off nt
	s_nop 0
	v_addc_co_u32_e32 v37, vcc, 0, v9, vcc
	global_load_dwordx4 v[36:39], v[36:37], off nt
	v_add_co_u32_e32 v40, vcc, s20, v8
	v_or_b32_e32 v4, 1, v16
	s_nop 0
	v_addc_co_u32_e32 v41, vcc, 0, v9, vcc
	global_load_dwordx4 v[40:43], v[40:41], off nt
	v_add_co_u32_e32 v44, vcc, s22, v8
	v_or_b32_e32 v64, 2, v16
	s_nop 0
	v_addc_co_u32_e32 v45, vcc, 0, v9, vcc
	global_load_dwordx4 v[44:47], v[44:45], off nt
	v_or_b32_e32 v65, 3, v16
	v_lshlrev_b32_e32 v66, 7, v12
	v_and_b32_e32 v48, 24, v31
	v_add_u32_e32 v51, s13, v66
	v_bitop3_b32 v53, v48, v16, v15 bitop3:0x36
	v_bitop3_b32 v54, v48, v4, v15 bitop3:0x36
	v_bitop3_b32 v55, v48, v64, v15 bitop3:0x36
	v_bitop3_b32 v48, v48, v65, v15 bitop3:0x36
	v_lshrrev_b32_e32 v49, 1, v30
	v_lshl_add_u32 v70, v48, 2, v51
	v_add_co_u32_e32 v48, vcc, s23, v8
	v_lshrrev_b32_e32 v50, 1, v29
	v_and_b32_e32 v56, 24, v49
	v_addc_co_u32_e32 v49, vcc, 0, v9, vcc
	v_and_b32_e32 v61, 24, v50
	v_lshl_add_u32 v67, v53, 2, v51
	v_lshl_add_u32 v68, v54, 2, v51
	v_lshl_add_u32 v69, v55, 2, v51
	global_load_dwordx4 v[48:51], v[48:49], off nt
	v_lshl_add_u32 v52, v30, 7, s13
	v_bitop3_b32 v53, v56, v16, v15 bitop3:0x36
	v_bitop3_b32 v54, v56, v4, v15 bitop3:0x36
	v_bitop3_b32 v55, v56, v64, v15 bitop3:0x36
	v_bitop3_b32 v56, v56, v65, v15 bitop3:0x36
	v_lshl_add_u32 v62, v53, 2, v52
	v_lshl_add_u32 v63, v54, 2, v52
	v_lshl_add_u32 v71, v55, 2, v52
	v_lshl_add_u32 v72, v56, 2, v52
	v_add_co_u32_e32 v52, vcc, s24, v8
	v_lshl_add_u32 v60, v29, 7, s13
	s_nop 0
	v_addc_co_u32_e32 v53, vcc, 0, v9, vcc
	v_bitop3_b32 v57, v61, v16, v15 bitop3:0x36
	v_add_co_u32_e32 v56, vcc, s25, v8
	v_lshl_add_u32 v73, v57, 2, v60
	s_nop 0
	v_addc_co_u32_e32 v57, vcc, 0, v9, vcc
	global_load_dwordx4 v[52:55], v[52:53], off nt
	s_nop 0
	global_load_dwordx4 v[56:59], v[56:57], off nt
	s_lshl_b32 s10, s10, 15
	s_add_u32 s6, s6, s10
	s_addc_u32 s7, s7, 0
	s_and_b32 s10, s8, 31
	s_mov_b32 s2, 0
	s_waitcnt vmcnt(7)
	ds_write_b32 v67, v0
	ds_write_b32 v68, v1
	ds_write_b32 v69, v2
	s_waitcnt vmcnt(6)
	ds_write_b32 v62, v32
	ds_write_b32 v63, v33
	ds_write_b32 v71, v34
	ds_write_b32 v72, v35
	s_waitcnt vmcnt(5)
	ds_write_b32 v73, v36
	v_bitop3_b32 v0, v61, v4, v15 bitop3:0x36
	v_lshl_add_u32 v0, v0, 2, v60
	v_lshrrev_b32_e32 v1, 1, v28
	v_and_b32_e32 v1, 24, v1
	v_bitop3_b32 v2, v1, v16, v15 bitop3:0x36
	ds_write_b32 v0, v37
	v_bitop3_b32 v0, v61, v64, v15 bitop3:0x36
	v_lshl_add_u32 v0, v0, 2, v60
	ds_write_b32 v0, v38
	v_bitop3_b32 v0, v61, v65, v15 bitop3:0x36
	v_lshl_add_u32 v0, v0, 2, v60
	ds_write_b32 v0, v39
	v_lshl_add_u32 v0, v28, 7, s13
	v_lshl_add_u32 v2, v2, 2, v0
	s_waitcnt vmcnt(4)
	ds_write_b32 v2, v40
	v_bitop3_b32 v2, v1, v4, v15 bitop3:0x36
	v_lshl_add_u32 v2, v2, 2, v0
	ds_write_b32 v2, v41
	v_bitop3_b32 v2, v1, v64, v15 bitop3:0x36
	v_bitop3_b32 v1, v1, v65, v15 bitop3:0x36
	v_lshl_add_u32 v2, v2, 2, v0
	v_lshl_add_u32 v0, v1, 2, v0
	v_lshrrev_b32_e32 v1, 1, v27
	v_and_b32_e32 v1, 24, v1
	ds_write_b32 v2, v42
	ds_write_b32 v0, v43
	v_lshl_add_u32 v0, v27, 7, s13
	v_bitop3_b32 v2, v1, v16, v15 bitop3:0x36
	v_lshl_add_u32 v2, v2, 2, v0
	s_waitcnt vmcnt(3)
	ds_write_b32 v2, v44
	v_bitop3_b32 v2, v1, v4, v15 bitop3:0x36
	v_lshl_add_u32 v2, v2, 2, v0
	ds_write_b32 v2, v45
	v_bitop3_b32 v2, v1, v64, v15 bitop3:0x36
	v_bitop3_b32 v1, v1, v65, v15 bitop3:0x36
	v_lshl_add_u32 v2, v2, 2, v0
	v_lshl_add_u32 v0, v1, 2, v0
	ds_write_b32 v0, v47
	v_add_co_u32_e32 v0, vcc, s26, v8
	ds_write_b32 v2, v46
	s_nop 0
	v_addc_co_u32_e32 v1, vcc, 0, v9, vcc
	global_load_dwordx4 v[32:35], v[0:1], off nt
	v_lshrrev_b32_e32 v0, 1, v26
	v_and_b32_e32 v40, 24, v0
	v_lshl_add_u32 v2, v26, 7, s13
	v_bitop3_b32 v0, v40, v16, v15 bitop3:0x36
	v_lshl_add_u32 v41, v0, 2, v2
	v_add_co_u32_e32 v0, vcc, s27, v8
	s_waitcnt vmcnt(3)
	ds_write_b32 v41, v48
	v_addc_co_u32_e32 v1, vcc, 0, v9, vcc
	global_load_dwordx4 v[36:39], v[0:1], off nt
	v_bitop3_b32 v0, v40, v4, v15 bitop3:0x36
	v_lshl_add_u32 v0, v0, 2, v2
	ds_write_b32 v0, v49
	v_bitop3_b32 v0, v40, v64, v15 bitop3:0x36
	v_lshl_add_u32 v0, v0, 2, v2
	ds_write_b32 v0, v50
	v_bitop3_b32 v0, v40, v65, v15 bitop3:0x36
	v_lshl_add_u32 v0, v0, 2, v2
	ds_write_b32 v0, v51
	v_add_co_u32_e32 v0, vcc, s28, v8
	v_lshl_add_u32 v2, v25, 7, s13
	s_nop 0
	v_addc_co_u32_e32 v1, vcc, 0, v9, vcc
	global_load_dwordx4 v[40:43], v[0:1], off nt
	v_lshrrev_b32_e32 v0, 1, v25
	v_and_b32_e32 v48, 24, v0
	v_bitop3_b32 v0, v48, v16, v15 bitop3:0x36
	v_lshl_add_u32 v0, v0, 2, v2
	s_waitcnt vmcnt(4)
	ds_write_b32 v0, v52
	v_bitop3_b32 v0, v48, v4, v15 bitop3:0x36
	v_lshl_add_u32 v0, v0, 2, v2
	ds_write_b32 v0, v53
	v_add_co_u32_e32 v0, vcc, s29, v8
	v_bitop3_b32 v49, v48, v64, v15 bitop3:0x36
	s_nop 0
	v_addc_co_u32_e32 v1, vcc, 0, v9, vcc
	global_load_dwordx4 v[44:47], v[0:1], off nt
	v_lshl_add_u32 v0, v49, 2, v2
	ds_write_b32 v0, v54
	v_bitop3_b32 v0, v48, v65, v15 bitop3:0x36
	v_lshl_add_u32 v0, v0, 2, v2
	ds_write_b32 v0, v55
	v_lshrrev_b32_e32 v0, 1, v24
	v_and_b32_e32 v52, 24, v0
	v_lshl_add_u32 v2, v24, 7, s13
	v_bitop3_b32 v0, v52, v16, v15 bitop3:0x36
	v_lshl_add_u32 v53, v0, 2, v2
	v_add_co_u32_e32 v0, vcc, s30, v8
	s_waitcnt vmcnt(4)
	ds_write_b32 v53, v56
	v_addc_co_u32_e32 v1, vcc, 0, v9, vcc
	global_load_dwordx4 v[48:51], v[0:1], off nt
	v_bitop3_b32 v0, v52, v4, v15 bitop3:0x36
	v_lshl_add_u32 v0, v0, 2, v2
	ds_write_b32 v0, v57
	v_bitop3_b32 v0, v52, v64, v15 bitop3:0x36
	v_lshl_add_u32 v0, v0, 2, v2
	ds_write_b32 v0, v58
	v_bitop3_b32 v0, v52, v65, v15 bitop3:0x36
	v_lshl_add_u32 v0, v0, 2, v2
	ds_write_b32 v0, v59
	v_add_co_u32_e32 v0, vcc, s31, v8
	v_readlane_b32 s49, v253, 5
	s_nop 0
	v_addc_co_u32_e32 v1, vcc, 0, v9, vcc
	global_load_dwordx4 v[52:55], v[0:1], off nt
	v_add_co_u32_e32 v0, vcc, s33, v8
	v_readlane_b32 s50, v253, 6
	s_nop 0
	v_addc_co_u32_e32 v1, vcc, 0, v9, vcc
	v_add_co_u32_e32 v8, vcc, s34, v8
	v_readlane_b32 s51, v253, 7
	s_nop 0
	v_addc_co_u32_e32 v9, vcc, 0, v9, vcc
	global_load_dwordx4 v[56:59], v[0:1], off nt
	global_load_dwordx4 v[60:63], v[8:9], off nt
	v_lshrrev_b32_e32 v1, 1, v23
	v_and_b32_e32 v1, 24, v1
	v_lshl_add_u32 v0, v23, 7, s13
	v_bitop3_b32 v2, v1, v16, v15 bitop3:0x36
	v_lshl_add_u32 v2, v2, 2, v0
	s_waitcnt vmcnt(7)
	ds_write_b32 v67, v32 offset:8192
	ds_write_b32 v68, v33 offset:8192
	ds_write_b32 v69, v34 offset:8192
	ds_write2st64_b32 v70, v3, v35 offset1:32
	v_or_b32_e32 v3, 4, v13
	v_or_b32_e32 v8, 5, v13
	s_waitcnt vmcnt(6)
	ds_write_b32 v2, v36
	v_bitop3_b32 v2, v1, v4, v15 bitop3:0x36
	v_lshl_add_u32 v2, v2, 2, v0
	ds_write_b32 v2, v37
	v_bitop3_b32 v2, v1, v64, v15 bitop3:0x36
	v_bitop3_b32 v1, v1, v65, v15 bitop3:0x36
	v_lshl_add_u32 v2, v2, 2, v0
	v_lshl_add_u32 v0, v1, 2, v0
	v_lshrrev_b32_e32 v1, 1, v22
	v_and_b32_e32 v1, 24, v1
	ds_write_b32 v2, v38
	ds_write_b32 v0, v39
	v_lshl_add_u32 v0, v22, 7, s13
	v_bitop3_b32 v2, v1, v16, v15 bitop3:0x36
	v_lshl_add_u32 v2, v2, 2, v0
	s_waitcnt vmcnt(5)
	ds_write_b32 v2, v40
	v_bitop3_b32 v2, v1, v4, v15 bitop3:0x36
	v_lshl_add_u32 v2, v2, 2, v0
	ds_write_b32 v2, v41
	v_bitop3_b32 v2, v1, v64, v15 bitop3:0x36
	v_bitop3_b32 v1, v1, v65, v15 bitop3:0x36
	v_lshl_add_u32 v2, v2, 2, v0
	v_lshl_add_u32 v0, v1, 2, v0
	v_lshrrev_b32_e32 v1, 1, v21
	v_and_b32_e32 v1, 24, v1
	ds_write_b32 v2, v42
	ds_write_b32 v0, v43
	v_lshl_add_u32 v0, v21, 7, s13
	v_bitop3_b32 v2, v1, v16, v15 bitop3:0x36
	v_lshl_add_u32 v2, v2, 2, v0
	s_waitcnt vmcnt(4)
	ds_write_b32 v2, v44
	v_bitop3_b32 v2, v1, v4, v15 bitop3:0x36
	v_lshl_add_u32 v2, v2, 2, v0
	ds_write_b32 v2, v45
	v_bitop3_b32 v2, v1, v64, v15 bitop3:0x36
	v_bitop3_b32 v1, v1, v65, v15 bitop3:0x36
	v_lshl_add_u32 v2, v2, 2, v0
	v_lshl_add_u32 v0, v1, 2, v0
	v_lshrrev_b32_e32 v1, 1, v20
	v_and_b32_e32 v1, 24, v1
	ds_write_b32 v2, v46
	ds_write_b32 v0, v47
	v_lshl_add_u32 v0, v20, 7, s13
	v_bitop3_b32 v2, v1, v16, v15 bitop3:0x36
	v_lshl_add_u32 v2, v2, 2, v0
	s_waitcnt vmcnt(3)
	ds_write_b32 v2, v48
	v_bitop3_b32 v2, v1, v4, v15 bitop3:0x36
	v_lshl_add_u32 v2, v2, 2, v0
	ds_write_b32 v2, v49
	v_bitop3_b32 v2, v1, v64, v15 bitop3:0x36
	v_bitop3_b32 v1, v1, v65, v15 bitop3:0x36
	v_lshl_add_u32 v2, v2, 2, v0
	v_lshl_add_u32 v0, v1, 2, v0
	v_lshrrev_b32_e32 v1, 1, v19
	v_and_b32_e32 v1, 24, v1
	ds_write_b32 v2, v50
	ds_write_b32 v0, v51
	v_lshl_add_u32 v0, v19, 7, s13
	v_bitop3_b32 v2, v1, v16, v15 bitop3:0x36
	v_lshl_add_u32 v2, v2, 2, v0
	s_waitcnt vmcnt(2)
	ds_write_b32 v2, v52
	v_bitop3_b32 v2, v1, v4, v15 bitop3:0x36
	v_lshl_add_u32 v2, v2, 2, v0
	ds_write_b32 v2, v53
	v_bitop3_b32 v2, v1, v64, v15 bitop3:0x36
	v_bitop3_b32 v1, v1, v65, v15 bitop3:0x36
	v_lshl_add_u32 v2, v2, 2, v0
	v_lshl_add_u32 v0, v1, 2, v0
	v_lshrrev_b32_e32 v1, 1, v18
	v_and_b32_e32 v1, 24, v1
	ds_write_b32 v2, v54
	ds_write_b32 v0, v55
	v_lshl_add_u32 v0, v18, 7, s13
	v_bitop3_b32 v2, v1, v16, v15 bitop3:0x36
	v_lshl_add_u32 v2, v2, 2, v0
	s_waitcnt vmcnt(1)
	ds_write_b32 v2, v56
	v_bitop3_b32 v2, v1, v4, v15 bitop3:0x36
	v_lshl_add_u32 v2, v2, 2, v0
	ds_write_b32 v2, v57
	v_bitop3_b32 v2, v1, v64, v15 bitop3:0x36
	v_bitop3_b32 v1, v1, v65, v15 bitop3:0x36
	v_lshl_add_u32 v2, v2, 2, v0
	v_lshl_add_u32 v0, v1, 2, v0
	v_lshrrev_b32_e32 v1, 1, v17
	v_and_b32_e32 v1, 24, v1
	ds_write_b32 v2, v58
	ds_write_b32 v0, v59
	v_lshl_add_u32 v0, v17, 7, s13
	v_bitop3_b32 v2, v1, v16, v15 bitop3:0x36
	v_lshl_add_u32 v2, v2, 2, v0
	s_waitcnt vmcnt(0)
	ds_write_b32 v2, v60
	v_bitop3_b32 v2, v1, v4, v15 bitop3:0x36
	v_lshl_add_u32 v2, v2, 2, v0
	ds_write_b32 v2, v61
	v_bitop3_b32 v2, v1, v64, v15 bitop3:0x36
	v_bitop3_b32 v1, v1, v65, v15 bitop3:0x36
	v_lshl_add_u32 v2, v2, 2, v0
	v_lshl_add_u32 v0, v1, 2, v0
	ds_write_b32 v2, v62
	ds_write_b32 v0, v63
	s_waitcnt lgkmcnt(0)
	v_or_b32_e32 v0, 1, v13
	v_or_b32_e32 v1, 2, v13
	v_or_b32_e32 v2, 3, v13
	v_or_b32_e32 v9, 6, v13
	v_or_b32_e32 v32, 7, v13
	v_lshl_add_u32 v33, s10, 12, v66
	v_add_u32_e32 v34, s9, v12
	v_readlane_b32 s52, v253, 8
	v_readlane_b32 s53, v253, 9
	v_readlane_b32 s54, v253, 10
	v_readlane_b32 s55, v253, 11
	v_readlane_b32 s56, v253, 12
	v_readlane_b32 s57, v253, 13
	v_readlane_b32 s58, v253, 14
	v_readlane_b32 s59, v253, 15
	v_readlane_b32 s62, v253, 18
	v_readlane_b32 s63, v253, 19

.LBB0_1069:
	s_mul_i32 s3, s2, s0
	s_sub_i32 s3, s5, s3
	s_xor_b32 s1, s6, s1
	s_add_i32 s5, s2, 1
	s_sub_i32 s6, s3, s0
	s_cmp_ge_u32 s3, s0
	s_cselect_b32 s2, s5, s2
	s_cselect_b32 s3, s6, s3
	s_add_i32 s5, s2, 1
	s_cmp_ge_u32 s3, s0
	s_cselect_b32 s0, s5, s2
	s_xor_b32 s0, s0, s1
	s_sub_i32 s0, s0, s1
	s_cmp_eq_u32 s0, s4
	s_cbranch_scc1 .LBB0_1086
	s_sub_i32 s2, s0, s4
	s_add_u32 s0, s94, 0x1000
	v_readlane_b32 s6, v253, 20
	s_addc_u32 s1, s95, 0
	s_lshl_b32 s4, s6, 14
	s_add_i32 s14, s4, 0
	s_cmp_lt_i32 s2, 0
	s_mul_i32 s12, s2, 3
	s_cselect_b64 s[4:5], -1, 0
	s_lshl_b32 s2, s6, 6
	s_sub_i32 s16, 0, s2
	s_add_u32 s17, s94, 0x7600000
	s_addc_u32 s18, s95, 0
	s_add_i32 s19, 0, 0x20180
	s_mov_b32 s3, 0
	v_mov_b32_e32 v5, 0
	v_mov_b32_e32 v10, s19
	s_mov_b32 s20, 0x8000
	s_mov_b32 s21, 0x10000
	s_mov_b32 s22, 0x18000
	s_mov_b32 s23, 0x20000
	s_mov_b32 s24, 0x28000
	s_mov_b32 s25, 0x30000
	s_mov_b32 s26, 0x38000
	s_mov_b32 s27, 0x40000
	s_mov_b32 s28, 0x48000
	s_mov_b32 s29, 0x50000
	s_mov_b32 s30, 0x58000
	s_mov_b32 s31, 0x60000
	s_mov_b32 s33, 0x68000
	s_mov_b32 s34, 0x70000
	s_mov_b32 s35, 0x78000
	s_mov_b32 s36, 0xc3e00000
	s_mov_b32 s37, 0x80000
	s_mov_b32 s38, 0x90000
	s_mov_b32 s39, 0xa0000
	s_mov_b32 s40, 0xb0000
	s_mov_b32 s41, 0xc0000
	s_mov_b32 s42, 0xd0000
	s_mov_b32 s43, 0xe0000
	s_mov_b32 s44, 0xf0000
	s_xor_b64 s[4:5], s[4:5], -1
	v_mov_b32_e32 v11, 0x43e00000
	s_mov_b32 s45, 0
	s_waitcnt vmcnt(0)
	s_barrier
	v_mbcnt_lo_u32_b32 v0, -1, 0
	v_mbcnt_hi_u32_b32 v0, -1, v0
	s_nop 0
	v_cmp_eq_u32_e32 vcc, s16, v0
	s_and_saveexec_b64 s[6:7], vcc
	s_cbranch_execz .LBB0_1077
	s_mov_b64 s[10:11], exec
	v_mbcnt_lo_u32_b32 v0, s10, 0
	v_mbcnt_hi_u32_b32 v0, s11, v0
	v_cmp_eq_u32_e32 vcc, 0, v0
	s_and_saveexec_b64 s[8:9], vcc
	s_cbranch_execz .LBB0_1076
	s_lshl_b32 s2, s12, 3
	v_mov_b32_e32 v1, s2
	global_atomic_add v1, v5, v1, s[0:1] sc0

.LBB0_1073:
	s_lshl_b32 s8, s45, 3
	s_add_i32 s8, s8, s100
	s_mov_b64 s[6:7], -1
	s_cmpk_gt_u32 s8, 0x5fff
	s_cbranch_scc1 .LBB0_1072
	v_readlane_b32 s2, v253, 20
	v_mbcnt_lo_u32_b32 v0, -1, 0
	v_mbcnt_hi_u32_b32 v0, -1, v0
	s_add_i32 s8, s8, s2
	v_ashrrev_i32_e32 v12, 3, v0
	v_and_b32_e32 v1, 7, v0
	v_lshlrev_b32_e32 v0, 3, v0
	s_cmpk_gt_i32 s8, 0x3fff
	v_lshlrev_b32_e32 v16, 2, v1
	v_lshlrev_b32_e32 v6, 4, v1
	v_and_b32_e32 v15, 7, v12
	v_lshrrev_b32_e32 v31, 1, v12
	v_add_u32_e32 v30, 8, v12
	v_add_u32_e32 v29, 16, v12
	v_add_u32_e32 v28, 24, v12
	v_add_u32_e32 v27, 32, v12
	v_add_u32_e32 v26, 40, v12
	v_add_u32_e32 v25, 48, v12
	v_add_u32_e32 v24, 56, v12
	v_add_u32_e32 v23, 0x48, v12
	v_add_u32_e32 v22, 0x50, v12
	v_add_u32_e32 v21, 0x58, v12
	v_add_u32_e32 v20, 0x60, v12
	v_add_u32_e32 v19, 0x68, v12
	v_add_u32_e32 v18, 0x70, v12
	v_add_u32_e32 v17, 0x78, v12
	v_and_b32_e32 v13, 24, v0
	v_lshl_add_u32 v14, v1, 11, s14
	s_cbranch_scc0 .LBB0_1082
	s_add_i32 s2, s8, 0xffffc000
	s_lshr_b32 s2, s2, 8
	s_addk_i32 s2, 0x60
	v_readlane_b32 s48, v253, 4
	s_lshl_b64 s[6:7], s[2:3], 20
	s_lshl_b64 s[10:11], s[2:3], 22
	v_readlane_b32 s60, v253, 16
	v_readlane_b32 s61, v253, 17
	s_add_u32 s2, s60, s10
	s_addc_u32 s11, s61, s11
	s_add_u32 s6, s13, s6
	s_addc_u32 s7, s15, s7
	s_lshl_b32 s9, s8, 5
	s_and_b32 s9, s9, 0x3e0
	s_bfe_u32 s10, s8, 0x30005
	s_lshl_b32 s46, s9, 2
	v_lshl_add_u32 v0, s10, 7, v12
	s_add_u32 s46, s2, s46
	s_addc_u32 s47, s11, 0
	v_mov_b32_e32 v7, v5
	v_ashrrev_i32_e32 v1, 31, v0
	v_lshl_add_u64 v[2:3], s[46:47], 0, v[6:7]
	v_lshlrev_b64 v[0:1], 12, v[0:1]
	v_lshl_add_u64 v[8:9], v[2:3], 0, v[0:1]
	v_add_co_u32_e32 v32, vcc, s20, v8
	global_load_dwordx4 v[0:3], v[8:9], off nt
	s_nop 0
	v_addc_co_u32_e32 v33, vcc, 0, v9, vcc
	v_add_co_u32_e32 v36, vcc, s21, v8
	global_load_dwordx4 v[32:35], v[32:33], off nt
	s_nop 0
	v_addc_co_u32_e32 v37, vcc, 0, v9, vcc
	global_load_dwordx4 v[36:39], v[36:37], off nt
	v_add_co_u32_e32 v40, vcc, s22, v8
	v_or_b32_e32 v4, 1, v16
	s_nop 0
	v_addc_co_u32_e32 v41, vcc, 0, v9, vcc
	global_load_dwordx4 v[40:43], v[40:41], off nt
	v_add_co_u32_e32 v44, vcc, s23, v8
	v_or_b32_e32 v64, 2, v16
	s_nop 0
	v_addc_co_u32_e32 v45, vcc, 0, v9, vcc
	global_load_dwordx4 v[44:47], v[44:45], off nt
	v_or_b32_e32 v65, 3, v16
	v_lshlrev_b32_e32 v66, 7, v12
	v_and_b32_e32 v48, 24, v31
	v_add_u32_e32 v51, s14, v66
	v_bitop3_b32 v53, v48, v16, v15 bitop3:0x36
	v_bitop3_b32 v54, v48, v4, v15 bitop3:0x36
	v_bitop3_b32 v55, v48, v64, v15 bitop3:0x36
	v_bitop3_b32 v48, v48, v65, v15 bitop3:0x36
	v_lshrrev_b32_e32 v49, 1, v30
	v_lshl_add_u32 v70, v48, 2, v51
	v_add_co_u32_e32 v48, vcc, s24, v8
	v_lshrrev_b32_e32 v50, 1, v29
	v_and_b32_e32 v56, 24, v49
	v_addc_co_u32_e32 v49, vcc, 0, v9, vcc
	v_and_b32_e32 v61, 24, v50
	v_lshl_add_u32 v67, v53, 2, v51
	v_lshl_add_u32 v68, v54, 2, v51
	v_lshl_add_u32 v69, v55, 2, v51
	global_load_dwordx4 v[48:51], v[48:49], off nt
	v_lshl_add_u32 v52, v30, 7, s14
	v_bitop3_b32 v53, v56, v16, v15 bitop3:0x36
	v_bitop3_b32 v54, v56, v4, v15 bitop3:0x36
	v_bitop3_b32 v55, v56, v64, v15 bitop3:0x36
	v_bitop3_b32 v56, v56, v65, v15 bitop3:0x36
	v_lshl_add_u32 v62, v53, 2, v52
	v_lshl_add_u32 v63, v54, 2, v52
	v_lshl_add_u32 v71, v55, 2, v52
	v_lshl_add_u32 v72, v56, 2, v52
	v_add_co_u32_e32 v52, vcc, s25, v8
	v_lshl_add_u32 v60, v29, 7, s14
	s_nop 0
	v_addc_co_u32_e32 v53, vcc, 0, v9, vcc
	v_bitop3_b32 v57, v61, v16, v15 bitop3:0x36
	v_add_co_u32_e32 v56, vcc, s26, v8
	v_lshl_add_u32 v73, v57, 2, v60
	s_nop 0
	v_addc_co_u32_e32 v57, vcc, 0, v9, vcc
	global_load_dwordx4 v[52:55], v[52:53], off nt
	s_nop 0
	global_load_dwordx4 v[56:59], v[56:57], off nt
	s_lshl_b32 s10, s10, 15
	s_add_u32 s6, s6, s10
	s_addc_u32 s7, s7, 0
	s_and_b32 s10, s8, 31
	s_mov_b32 s2, 0
	s_waitcnt vmcnt(7)
	ds_write_b32 v67, v0
	ds_write_b32 v68, v1
	ds_write_b32 v69, v2
	s_waitcnt vmcnt(6)
	ds_write_b32 v62, v32
	ds_write_b32 v63, v33
	ds_write_b32 v71, v34
	ds_write_b32 v72, v35
	s_waitcnt vmcnt(5)
	ds_write_b32 v73, v36
	v_bitop3_b32 v0, v61, v4, v15 bitop3:0x36
	v_lshl_add_u32 v0, v0, 2, v60
	v_lshrrev_b32_e32 v1, 1, v28
	v_and_b32_e32 v1, 24, v1
	v_bitop3_b32 v2, v1, v16, v15 bitop3:0x36
	ds_write_b32 v0, v37
	v_bitop3_b32 v0, v61, v64, v15 bitop3:0x36
	v_lshl_add_u32 v0, v0, 2, v60
	ds_write_b32 v0, v38
	v_bitop3_b32 v0, v61, v65, v15 bitop3:0x36
	v_lshl_add_u32 v0, v0, 2, v60
	ds_write_b32 v0, v39
	v_lshl_add_u32 v0, v28, 7, s14
	v_lshl_add_u32 v2, v2, 2, v0
	s_waitcnt vmcnt(4)
	ds_write_b32 v2, v40
	v_bitop3_b32 v2, v1, v4, v15 bitop3:0x36
	v_lshl_add_u32 v2, v2, 2, v0
	ds_write_b32 v2, v41
	v_bitop3_b32 v2, v1, v64, v15 bitop3:0x36
	v_bitop3_b32 v1, v1, v65, v15 bitop3:0x36
	v_lshl_add_u32 v2, v2, 2, v0
	v_lshl_add_u32 v0, v1, 2, v0
	v_lshrrev_b32_e32 v1, 1, v27
	v_and_b32_e32 v1, 24, v1
	ds_write_b32 v2, v42
	ds_write_b32 v0, v43
	v_lshl_add_u32 v0, v27, 7, s14
	v_bitop3_b32 v2, v1, v16, v15 bitop3:0x36
	v_lshl_add_u32 v2, v2, 2, v0
	s_waitcnt vmcnt(3)
	ds_write_b32 v2, v44
	v_bitop3_b32 v2, v1, v4, v15 bitop3:0x36
	v_lshl_add_u32 v2, v2, 2, v0
	ds_write_b32 v2, v45
	v_bitop3_b32 v2, v1, v64, v15 bitop3:0x36
	v_bitop3_b32 v1, v1, v65, v15 bitop3:0x36
	v_lshl_add_u32 v2, v2, 2, v0
	v_lshl_add_u32 v0, v1, 2, v0
	ds_write_b32 v0, v47
	v_add_co_u32_e32 v0, vcc, s27, v8
	ds_write_b32 v2, v46
	s_nop 0
	v_addc_co_u32_e32 v1, vcc, 0, v9, vcc
	global_load_dwordx4 v[32:35], v[0:1], off nt
	v_lshrrev_b32_e32 v0, 1, v26
	v_and_b32_e32 v40, 24, v0
	v_lshl_add_u32 v2, v26, 7, s14
	v_bitop3_b32 v0, v40, v16, v15 bitop3:0x36
	v_lshl_add_u32 v41, v0, 2, v2
	v_add_co_u32_e32 v0, vcc, s28, v8
	s_waitcnt vmcnt(3)
	ds_write_b32 v41, v48
	v_addc_co_u32_e32 v1, vcc, 0, v9, vcc
	global_load_dwordx4 v[36:39], v[0:1], off nt
	v_bitop3_b32 v0, v40, v4, v15 bitop3:0x36
	v_lshl_add_u32 v0, v0, 2, v2
	ds_write_b32 v0, v49
	v_bitop3_b32 v0, v40, v64, v15 bitop3:0x36
	v_lshl_add_u32 v0, v0, 2, v2
	ds_write_b32 v0, v50
	v_bitop3_b32 v0, v40, v65, v15 bitop3:0x36
	v_lshl_add_u32 v0, v0, 2, v2
	ds_write_b32 v0, v51
	v_add_co_u32_e32 v0, vcc, s29, v8
	v_lshl_add_u32 v2, v25, 7, s14
	s_nop 0
	v_addc_co_u32_e32 v1, vcc, 0, v9, vcc
	global_load_dwordx4 v[40:43], v[0:1], off nt
	v_lshrrev_b32_e32 v0, 1, v25
	v_and_b32_e32 v48, 24, v0
	v_bitop3_b32 v0, v48, v16, v15 bitop3:0x36
	v_lshl_add_u32 v0, v0, 2, v2
	s_waitcnt vmcnt(4)
	ds_write_b32 v0, v52
	v_bitop3_b32 v0, v48, v4, v15 bitop3:0x36
	v_lshl_add_u32 v0, v0, 2, v2
	ds_write_b32 v0, v53
	v_add_co_u32_e32 v0, vcc, s30, v8
	v_bitop3_b32 v49, v48, v64, v15 bitop3:0x36
	s_nop 0
	v_addc_co_u32_e32 v1, vcc, 0, v9, vcc
	global_load_dwordx4 v[44:47], v[0:1], off nt
	v_lshl_add_u32 v0, v49, 2, v2
	ds_write_b32 v0, v54
	v_bitop3_b32 v0, v48, v65, v15 bitop3:0x36
	v_lshl_add_u32 v0, v0, 2, v2
	ds_write_b32 v0, v55
	v_lshrrev_b32_e32 v0, 1, v24
	v_and_b32_e32 v52, 24, v0
	v_lshl_add_u32 v2, v24, 7, s14
	v_bitop3_b32 v0, v52, v16, v15 bitop3:0x36
	v_lshl_add_u32 v53, v0, 2, v2
	v_add_co_u32_e32 v0, vcc, s31, v8
	s_waitcnt vmcnt(4)
	ds_write_b32 v53, v56
	v_addc_co_u32_e32 v1, vcc, 0, v9, vcc
	global_load_dwordx4 v[48:51], v[0:1], off nt
	v_bitop3_b32 v0, v52, v4, v15 bitop3:0x36
	v_lshl_add_u32 v0, v0, 2, v2
	ds_write_b32 v0, v57
	v_bitop3_b32 v0, v52, v64, v15 bitop3:0x36
	v_lshl_add_u32 v0, v0, 2, v2
	ds_write_b32 v0, v58
	v_bitop3_b32 v0, v52, v65, v15 bitop3:0x36
	v_lshl_add_u32 v0, v0, 2, v2
	ds_write_b32 v0, v59
	v_add_co_u32_e32 v0, vcc, s33, v8
	v_readlane_b32 s49, v253, 5
	s_nop 0
	v_addc_co_u32_e32 v1, vcc, 0, v9, vcc
	global_load_dwordx4 v[52:55], v[0:1], off nt
	v_add_co_u32_e32 v0, vcc, s34, v8
	v_readlane_b32 s50, v253, 6
	s_nop 0
	v_addc_co_u32_e32 v1, vcc, 0, v9, vcc
	v_add_co_u32_e32 v8, vcc, s35, v8
	v_readlane_b32 s51, v253, 7
	s_nop 0
	v_addc_co_u32_e32 v9, vcc, 0, v9, vcc
	global_load_dwordx4 v[56:59], v[0:1], off nt
	global_load_dwordx4 v[60:63], v[8:9], off nt
	v_lshrrev_b32_e32 v1, 1, v23
	v_and_b32_e32 v1, 24, v1
	v_lshl_add_u32 v0, v23, 7, s14
	v_bitop3_b32 v2, v1, v16, v15 bitop3:0x36
	v_lshl_add_u32 v2, v2, 2, v0
	s_waitcnt vmcnt(7)
	ds_write_b32 v67, v32 offset:8192
	ds_write_b32 v68, v33 offset:8192
	ds_write_b32 v69, v34 offset:8192
	ds_write2st64_b32 v70, v3, v35 offset1:32
	v_or_b32_e32 v3, 4, v13
	v_or_b32_e32 v8, 5, v13
	s_waitcnt vmcnt(6)
	ds_write_b32 v2, v36
	v_bitop3_b32 v2, v1, v4, v15 bitop3:0x36
	v_lshl_add_u32 v2, v2, 2, v0
	ds_write_b32 v2, v37
	v_bitop3_b32 v2, v1, v64, v15 bitop3:0x36
	v_bitop3_b32 v1, v1, v65, v15 bitop3:0x36
	v_lshl_add_u32 v2, v2, 2, v0
	v_lshl_add_u32 v0, v1, 2, v0
	v_lshrrev_b32_e32 v1, 1, v22
	v_and_b32_e32 v1, 24, v1
	ds_write_b32 v2, v38
	ds_write_b32 v0, v39
	v_lshl_add_u32 v0, v22, 7, s14
	v_bitop3_b32 v2, v1, v16, v15 bitop3:0x36
	v_lshl_add_u32 v2, v2, 2, v0
	s_waitcnt vmcnt(5)
	ds_write_b32 v2, v40
	v_bitop3_b32 v2, v1, v4, v15 bitop3:0x36
	v_lshl_add_u32 v2, v2, 2, v0
	ds_write_b32 v2, v41
	v_bitop3_b32 v2, v1, v64, v15 bitop3:0x36
	v_bitop3_b32 v1, v1, v65, v15 bitop3:0x36
	v_lshl_add_u32 v2, v2, 2, v0
	v_lshl_add_u32 v0, v1, 2, v0
	v_lshrrev_b32_e32 v1, 1, v21
	v_and_b32_e32 v1, 24, v1
	ds_write_b32 v2, v42
	ds_write_b32 v0, v43
	v_lshl_add_u32 v0, v21, 7, s14
	v_bitop3_b32 v2, v1, v16, v15 bitop3:0x36
	v_lshl_add_u32 v2, v2, 2, v0
	s_waitcnt vmcnt(4)
	ds_write_b32 v2, v44
	v_bitop3_b32 v2, v1, v4, v15 bitop3:0x36
	v_lshl_add_u32 v2, v2, 2, v0
	ds_write_b32 v2, v45
	v_bitop3_b32 v2, v1, v64, v15 bitop3:0x36
	v_bitop3_b32 v1, v1, v65, v15 bitop3:0x36
	v_lshl_add_u32 v2, v2, 2, v0
	v_lshl_add_u32 v0, v1, 2, v0
	v_lshrrev_b32_e32 v1, 1, v20
	v_and_b32_e32 v1, 24, v1
	ds_write_b32 v2, v46
	ds_write_b32 v0, v47
	v_lshl_add_u32 v0, v20, 7, s14
	v_bitop3_b32 v2, v1, v16, v15 bitop3:0x36
	v_lshl_add_u32 v2, v2, 2, v0
	s_waitcnt vmcnt(3)
	ds_write_b32 v2, v48
	v_bitop3_b32 v2, v1, v4, v15 bitop3:0x36
	v_lshl_add_u32 v2, v2, 2, v0
	ds_write_b32 v2, v49
	v_bitop3_b32 v2, v1, v64, v15 bitop3:0x36
	v_bitop3_b32 v1, v1, v65, v15 bitop3:0x36
	v_lshl_add_u32 v2, v2, 2, v0
	v_lshl_add_u32 v0, v1, 2, v0
	v_lshrrev_b32_e32 v1, 1, v19
	v_and_b32_e32 v1, 24, v1
	ds_write_b32 v2, v50
	ds_write_b32 v0, v51
	v_lshl_add_u32 v0, v19, 7, s14
	v_bitop3_b32 v2, v1, v16, v15 bitop3:0x36
	v_lshl_add_u32 v2, v2, 2, v0
	s_waitcnt vmcnt(2)
	ds_write_b32 v2, v52
	v_bitop3_b32 v2, v1, v4, v15 bitop3:0x36
	v_lshl_add_u32 v2, v2, 2, v0
	ds_write_b32 v2, v53
	v_bitop3_b32 v2, v1, v64, v15 bitop3:0x36
	v_bitop3_b32 v1, v1, v65, v15 bitop3:0x36
	v_lshl_add_u32 v2, v2, 2, v0
	v_lshl_add_u32 v0, v1, 2, v0
	v_lshrrev_b32_e32 v1, 1, v18
	v_and_b32_e32 v1, 24, v1
	ds_write_b32 v2, v54
	ds_write_b32 v0, v55
	v_lshl_add_u32 v0, v18, 7, s14
	v_bitop3_b32 v2, v1, v16, v15 bitop3:0x36
	v_lshl_add_u32 v2, v2, 2, v0
	s_waitcnt vmcnt(1)
	ds_write_b32 v2, v56
	v_bitop3_b32 v2, v1, v4, v15 bitop3:0x36
	v_lshl_add_u32 v2, v2, 2, v0
	ds_write_b32 v2, v57
	v_bitop3_b32 v2, v1, v64, v15 bitop3:0x36
	v_bitop3_b32 v1, v1, v65, v15 bitop3:0x36
	v_lshl_add_u32 v2, v2, 2, v0
	v_lshl_add_u32 v0, v1, 2, v0
	v_lshrrev_b32_e32 v1, 1, v17
	v_and_b32_e32 v1, 24, v1
	ds_write_b32 v2, v58
	ds_write_b32 v0, v59
	v_lshl_add_u32 v0, v17, 7, s14
	v_bitop3_b32 v2, v1, v16, v15 bitop3:0x36
	v_lshl_add_u32 v2, v2, 2, v0
	s_waitcnt vmcnt(0)
	ds_write_b32 v2, v60
	v_bitop3_b32 v2, v1, v4, v15 bitop3:0x36
	v_lshl_add_u32 v2, v2, 2, v0
	ds_write_b32 v2, v61
	v_bitop3_b32 v2, v1, v64, v15 bitop3:0x36
	v_bitop3_b32 v1, v1, v65, v15 bitop3:0x36
	v_lshl_add_u32 v2, v2, 2, v0
	v_lshl_add_u32 v0, v1, 2, v0
	ds_write_b32 v2, v62
	ds_write_b32 v0, v63
	s_waitcnt lgkmcnt(0)
	v_or_b32_e32 v0, 1, v13
	v_or_b32_e32 v1, 2, v13
	v_or_b32_e32 v2, 3, v13
	v_or_b32_e32 v9, 6, v13
	v_or_b32_e32 v32, 7, v13
	v_lshl_add_u32 v33, s10, 12, v66
	v_add_u32_e32 v34, s9, v12
	v_readlane_b32 s52, v253, 8
	v_readlane_b32 s53, v253, 9
	v_readlane_b32 s54, v253, 10
	v_readlane_b32 s55, v253, 11
	v_readlane_b32 s56, v253, 12
	v_readlane_b32 s57, v253, 13
	v_readlane_b32 s58, v253, 14
	v_readlane_b32 s59, v253, 15
	v_readlane_b32 s62, v253, 18
	v_readlane_b32 s63, v253, 19
